# right-sized helper share: 384 items per busy XCD group after E1 and 192 after E2 (their overrun would sit on the critical path; the lightly loaded groups have headroom)
# baseline (speedup 1.0000x reference)
;     __device__ bool next(int i, Unit& u) const {
;         const long L = (long)i * G + c; int wgid;
;         if (aligned) {
;             const int ng = (nM + WGM - 1) / WGM, gq = ng / NXCD, gr = ng % NXCD, xcd = (int)(L % NXCD); const long off = L / NXCD;
;             const int g0 = xcd * gq + (xcd < gr ? xcd : gr), g1 = g0 + gq + (xcd < gr ? 1 : 0);
;             const long w = (long)g0 * (WGM * 4) + off, wend = (long)g1 * (WGM * 4) < nwg ? (long)g1 * (WGM * 4) : nwg;
;             if (w >= wend) return false;
;             wgid = (int)w;
; __global__ void __launch_bounds__(NWAVES * 64, 2) mk_fwd(Args args) {
;     ...
;         {
;             const int step = G * NWAVES; int it0 = CONV_EARLY + bid * NWAVES + wave;
;             ConvDesc dA, dB; f32x4 vA[16], vB[16];
;             if (it0 < NCONV_ITEMS) { CONV_DECODE(dA, it0); conv_load(vA, dA, lane); }
; #pragma unroll 1
;             for (; it0 < NCONV_ITEMS; it0 += 2 * step) {
;                 const bool hasB = it0 + step < NCONV_ITEMS, hasA2 = it0 + 2 * step < NCONV_ITEMS;
;                 if (hasB) { CONV_DECODE(dB, it0 + step); conv_load(vB, dB, lane); }
;                 conv_process(vA, dA, scr, lane);
;                 if (hasA2) { CONV_DECODE(dA, it0 + 2 * step); conv_load(vA, dA, lane); }
;                 if (hasB) conv_process(vB, dB, scr, lane);
;             }
.LBB0_1541:
	v_mov_b32_e32 v252, 0x27c80
	ds_read_b32 v252, v252
	s_waitcnt lgkmcnt(0)
	v_readfirstlane_b32 s100, v252
	s_nop 1
	s_lshr_b32 s100, s100, 8
	s_add_i32 s100, s100, 3
	s_lshr_b32 s100, s100, 2
	s_and_b32 s100, s100, 7
	s_cmp_eq_u32 s100, 0
	s_cbranch_scc1 .LslotA_skip
	s_cmp_ge_u32 s100, 6
	s_cbranch_scc1 .LslotA_skip
	s_and_b32 s98, s83, 7
	s_cmp_ge_u32 s98, s100
	s_cbranch_scc1 .LslotA_skip
	s_lshr_b32 s101, s83, 3
	s_cmp_lt_u32 s101, 16
	s_cbranch_scc1 .LslotA_skip
	s_lshl_b32 s98, s98, 4
	s_add_i32 s98, s98, s101
	s_sub_i32 s98, s98, 16
	s_lshl_b32 s100, s100, 4
	s_add_i32 s98, s98, 0x600
	v_writelane_b32 v253, s14, 0
	v_writelane_b32 v253, s15, 1
	v_writelane_b32 v253, s16, 2
	v_writelane_b32 v253, s17, 3
	v_writelane_b32 v253, s19, 4
	v_writelane_b32 v253, s21, 5
	v_writelane_b32 v253, s57, 6
	v_mov_b32_e32 v254, v3
	s_lshl_b32 s101, s100, 4
	s_lshl_b32 s99, s100, 3
	s_add_i32 s101, s101, s99
	s_add_i32 s101, s101, 0x3900
	s_mov_b32 s99, 5
	s_lshl_b32 s50, s98, 3
	s_add_i32 s50, s50, s85
	s_lshl_b32 s49, s98, 9
	s_lshl_b32 s48, s100, 3
	s_lshl_b32 s2, s100, 9
	s_mov_b64 s[0:1], s[78:79]
	s_mul_i32 s3, s85, 0x4100
	s_lshl_b32 s88, s85, 6
	s_branch .Lconv_entry

;     __device__ bool next(int i, Unit& u) const {
;         const long L = (long)i * G + c; int wgid;
;         if (aligned) {
;             const int ng = (nM + WGM - 1) / WGM, gq = ng / NXCD, gr = ng % NXCD, xcd = (int)(L % NXCD); const long off = L / NXCD;
;             const int g0 = xcd * gq + (xcd < gr ? xcd : gr), g1 = g0 + gq + (xcd < gr ? 1 : 0);
;             const long w = (long)g0 * (WGM * 4) + off, wend = (long)g1 * (WGM * 4) < nwg ? (long)g1 * (WGM * 4) : nwg;
;             if (w >= wend) return false;
;             wgid = (int)w;
; __global__ void __launch_bounds__(NWAVES * 64, 2) mk_fwd(Args args) {
;     ...
;         {
;             const int step = G * NWAVES; int it0 = CONV_EARLY + bid * NWAVES + wave;
;             ConvDesc dA, dB; f32x4 vA[16], vB[16];
;             if (it0 < NCONV_ITEMS) { CONV_DECODE(dA, it0); conv_load(vA, dA, lane); }
; #pragma unroll 1
;             for (; it0 < NCONV_ITEMS; it0 += 2 * step) {
;                 const bool hasB = it0 + step < NCONV_ITEMS, hasA2 = it0 + 2 * step < NCONV_ITEMS;
;                 if (hasB) { CONV_DECODE(dB, it0 + step); conv_load(vB, dB, lane); }
;                 conv_process(vA, dA, scr, lane);
;                 if (hasA2) { CONV_DECODE(dA, it0 + 2 * step); conv_load(vA, dA, lane); }
;                 if (hasB) conv_process(vB, dB, scr, lane);
;             }
.LBB0_1657:
	s_waitcnt vmcnt(0) lgkmcnt(0)
	s_barrier
	v_mov_b32_e32 v252, 0x27c80
	ds_read_b32 v252, v252
	s_waitcnt lgkmcnt(0)
	v_readfirstlane_b32 s100, v252
	s_nop 1
	s_lshr_b32 s100, s100, 8
	s_add_i32 s100, s100, 3
	s_lshr_b32 s100, s100, 2
	s_and_b32 s100, s100, 7
	s_and_b32 s98, s83, 7
	s_cmp_eq_u32 s100, 0
	s_cbranch_scc1 .Lsp_all
	s_cmp_ge_u32 s100, 6
	s_cbranch_scc1 .Lsp_all
	s_lshr_b32 s101, s83, 3
	s_cmp_lt_u32 s98, s100
	s_cbranch_scc1 .Lsp_heavy
	s_sub_i32 s98, s98, s100
	s_lshl_b32 s98, s98, 5
	s_add_i32 s98, s98, s101
	s_lshl_b32 s101, s100, 6
	s_add_i32 s98, s98, s101
	s_lshl_b32 s101, s100, 3
	s_add_i32 s98, s98, s101
	s_sub_i32 s100, 8, s100
	s_lshl_b32 s100, s100, 5
	s_add_i32 s98, s98, 0x600
	s_branch .Lsp_go
.Lsp_heavy:
	s_cmp_lt_u32 s101, 16
	s_cbranch_scc1 .Lq_done
	s_lshl_b32 s98, s98, 4
	s_add_i32 s98, s98, s101
	s_sub_i32 s98, s98, 16
	s_lshl_b32 s100, s100, 4
	s_lshl_b32 s101, s100, 1
	s_add_i32 s98, s98, s101
	s_add_i32 s98, s98, s100
	s_add_i32 s98, s98, 0x600
	s_lshl_b32 s101, s100, 5
	s_lshl_b32 s99, s100, 2
	s_add_i32 s101, s101, s99
	s_add_i32 s101, s101, 0x3900
	s_mov_b32 s99, 2
	s_lshl_b32 s50, s98, 3
	s_add_i32 s50, s50, s85
	s_lshl_b32 s49, s98, 9
	s_lshl_b32 s48, s100, 3
	s_lshl_b32 s2, s100, 9
	s_mov_b64 s[0:1], s[78:79]
	s_mul_i32 s3, s85, 0x4100
	s_lshl_b32 s88, s85, 6
	s_branch .Lconv_entry
